# v39 + hand-written P4 epilogue (rolling residual loads, dwordx4 stores via permlane swaps)
# speedup vs baseline: 1.0057x; 1.0057x over previous
.LBB0_565:
	s_andn2_b64 vcc, exec, s[4:5]
	s_mov_b64 s[4:5], -1
	s_ashr_i32 s21, s28, 4
	s_mul_hi_i32 s23, s21, 0x18000
	s_mul_i32 s21, s21, 0x18000
	s_add_u32 s30, s45, s21
	s_addc_u32 s31, s46, s23
	v_lshl_or_b32 v224, s54, 8, v197
	v_mov_b32_e32 v225, 0
	v_lshl_add_u64 v[226:227], v[224:225], 2, s[30:31]
	global_load_dwordx4 v[200:203], v[226:227], off
	global_load_dwordx4 v[204:207], v[226:227], off offset:64
	global_load_dwordx4 v[208:211], v[226:227], off offset:512
	global_load_dwordx4 v[212:215], v[226:227], off offset:576
	v_lshl_add_u32 v228, s28, 8, v180
	v_mov_b32_e32 v229, 0
	v_lshlrev_b64 v[216:217], 14, v[228:229]
	v_lshl_add_u64 v[216:217], v[216:217], 0, s[8:9]
	v_lshl_add_u64 v[216:217], v[224:225], 2, v[216:217]
	v_lshlrev_b64 v[218:219], 13, v[228:229]
	v_lshl_add_u64 v[218:219], v[218:219], 0, s[12:13]
	v_and_b32_e32 v230, 12, v197
	v_add_u32_e32 v230, v230, v224
	v_mov_b32_e32 v231, 0
	v_lshl_add_u64 v[218:219], v[230:231], 1, v[218:219]
	s_mov_b32 s30, 0x0
	s_mov_b32 s31, 0
	v_lshl_add_u64 v[220:221], v[216:217], 0, s[30:31]
	global_load_dwordx4 v[0:3], v[220:221], off
	global_load_dwordx4 v[4:7], v[220:221], off offset:64
	s_mov_b32 s30, 0x0
	s_mov_b32 s31, 0
	v_lshl_add_u64 v[220:221], v[216:217], 0, s[30:31]
	global_load_dwordx4 v[8:11], v[220:221], off offset:512
	global_load_dwordx4 v[12:15], v[220:221], off offset:576
	s_mov_b32 s30, 0x40000
	s_mov_b32 s31, 0
	v_lshl_add_u64 v[220:221], v[216:217], 0, s[30:31]
	global_load_dwordx4 v[16:19], v[220:221], off
	global_load_dwordx4 v[20:23], v[220:221], off offset:64
	s_mov_b32 s30, 0x40000
	s_mov_b32 s31, 0
	v_lshl_add_u64 v[220:221], v[216:217], 0, s[30:31]
	global_load_dwordx4 v[24:27], v[220:221], off offset:512
	global_load_dwordx4 v[28:31], v[220:221], off offset:576
	s_mov_b32 s30, 0x80000
	s_mov_b32 s31, 0
	v_lshl_add_u64 v[220:221], v[216:217], 0, s[30:31]
	global_load_dwordx4 v[172:175], v[220:221], off
	global_load_dwordx4 v[176:179], v[220:221], off offset:64
	s_waitcnt vmcnt(10)
	v_mul_f32_e32 v200, s18, v200
	v_mul_f32_e32 v201, s18, v201
	v_mul_f32_e32 v202, s18, v202
	v_mul_f32_e32 v203, s18, v203
	v_mul_f32_e32 v204, s18, v204
	v_mul_f32_e32 v205, s18, v205
	v_mul_f32_e32 v206, s18, v206
	v_mul_f32_e32 v207, s18, v207
	v_mul_f32_e32 v208, s18, v208
	v_mul_f32_e32 v209, s18, v209
	v_mul_f32_e32 v210, s18, v210
	v_mul_f32_e32 v211, s18, v211
	v_mul_f32_e32 v212, s18, v212
	v_mul_f32_e32 v213, s18, v213
	v_mul_f32_e32 v214, s18, v214
	v_mul_f32_e32 v215, s18, v215
	s_waitcnt vmcnt(8)
	v_fma_f32 v0, v156, v200, v0
	v_fma_f32 v1, v157, v201, v1
	v_fma_f32 v2, v158, v202, v2
	v_fma_f32 v3, v159, v203, v3
	v_fma_f32 v4, v152, v204, v4
	v_fma_f32 v5, v153, v205, v5
	v_fma_f32 v6, v154, v206, v6
	v_fma_f32 v7, v155, v207, v7
	v_cvt_pk_bf16_f32 v0, v0, v1
	v_cvt_pk_bf16_f32 v1, v2, v3
	v_cvt_pk_bf16_f32 v2, v4, v5
	v_cvt_pk_bf16_f32 v3, v6, v7
	s_mov_b32 s30, 0x0
	s_mov_b32 s31, 0
	v_lshl_add_u64 v[222:223], v[218:219], 0, s[30:31]
	s_nop 1
	v_permlane32_swap_b32_e32 v0, v2
	v_permlane32_swap_b32_e32 v1, v3
	s_nop 1
	v_permlane16_swap_b32_e32 v0, v2
	v_permlane16_swap_b32_e32 v1, v3
	global_store_dwordx4 v[222:223], v[0:3], off
	s_mov_b32 s30, 0x80000
	s_mov_b32 s31, 0
	v_lshl_add_u64 v[220:221], v[216:217], 0, s[30:31]
	global_load_dwordx4 v[0:3], v[220:221], off offset:512
	global_load_dwordx4 v[4:7], v[220:221], off offset:576
	s_waitcnt vmcnt(9)
	v_fma_f32 v8, v140, v208, v8
	v_fma_f32 v9, v141, v209, v9
	v_fma_f32 v10, v142, v210, v10
	v_fma_f32 v11, v143, v211, v11
	v_fma_f32 v12, v136, v212, v12
	v_fma_f32 v13, v137, v213, v13
	v_fma_f32 v14, v138, v214, v14
	v_fma_f32 v15, v139, v215, v15
	v_cvt_pk_bf16_f32 v8, v8, v9
	v_cvt_pk_bf16_f32 v9, v10, v11
	v_cvt_pk_bf16_f32 v10, v12, v13
	v_cvt_pk_bf16_f32 v11, v14, v15
	s_mov_b32 s30, 0x0
	s_mov_b32 s31, 0
	v_lshl_add_u64 v[222:223], v[218:219], 0, s[30:31]
	s_nop 1
	v_permlane32_swap_b32_e32 v8, v10
	v_permlane32_swap_b32_e32 v9, v11
	s_nop 1
	v_permlane16_swap_b32_e32 v8, v10
	v_permlane16_swap_b32_e32 v9, v11
	global_store_dwordx4 v[222:223], v[8:11], off offset:256
	s_mov_b32 s30, 0xc0000
	s_mov_b32 s31, 0
	v_lshl_add_u64 v[220:221], v[216:217], 0, s[30:31]
	global_load_dwordx4 v[8:11], v[220:221], off
	global_load_dwordx4 v[12:15], v[220:221], off offset:64
	s_waitcnt vmcnt(10)
	v_fma_f32 v16, v148, v200, v16
	v_fma_f32 v17, v149, v201, v17
	v_fma_f32 v18, v150, v202, v18
	v_fma_f32 v19, v151, v203, v19
	v_fma_f32 v20, v144, v204, v20
	v_fma_f32 v21, v145, v205, v21
	v_fma_f32 v22, v146, v206, v22
	v_fma_f32 v23, v147, v207, v23
	v_cvt_pk_bf16_f32 v16, v16, v17
	v_cvt_pk_bf16_f32 v17, v18, v19
	v_cvt_pk_bf16_f32 v18, v20, v21
	v_cvt_pk_bf16_f32 v19, v22, v23
	s_mov_b32 s30, 0x20000
	s_mov_b32 s31, 0
	v_lshl_add_u64 v[222:223], v[218:219], 0, s[30:31]
	s_nop 1
	v_permlane32_swap_b32_e32 v16, v18
	v_permlane32_swap_b32_e32 v17, v19
	s_nop 1
	v_permlane16_swap_b32_e32 v16, v18
	v_permlane16_swap_b32_e32 v17, v19
	global_store_dwordx4 v[222:223], v[16:19], off
	s_mov_b32 s30, 0xc0000
	s_mov_b32 s31, 0
	v_lshl_add_u64 v[220:221], v[216:217], 0, s[30:31]
	global_load_dwordx4 v[16:19], v[220:221], off offset:512
	global_load_dwordx4 v[20:23], v[220:221], off offset:576
	s_waitcnt vmcnt(11)
	v_fma_f32 v24, v132, v208, v24
	v_fma_f32 v25, v133, v209, v25
	v_fma_f32 v26, v134, v210, v26
	v_fma_f32 v27, v135, v211, v27
	v_fma_f32 v28, v128, v212, v28
	v_fma_f32 v29, v129, v213, v29
	v_fma_f32 v30, v130, v214, v30
	v_fma_f32 v31, v131, v215, v31
	v_cvt_pk_bf16_f32 v24, v24, v25
	v_cvt_pk_bf16_f32 v25, v26, v27
	v_cvt_pk_bf16_f32 v26, v28, v29
	v_cvt_pk_bf16_f32 v27, v30, v31
	s_mov_b32 s30, 0x20000
	s_mov_b32 s31, 0
	v_lshl_add_u64 v[222:223], v[218:219], 0, s[30:31]
	s_nop 1
	v_permlane32_swap_b32_e32 v24, v26
	v_permlane32_swap_b32_e32 v25, v27
	s_nop 1
	v_permlane16_swap_b32_e32 v24, v26
	v_permlane16_swap_b32_e32 v25, v27
	global_store_dwordx4 v[222:223], v[24:27], off offset:256
	s_mov_b32 s30, 0x200000
	s_mov_b32 s31, 0
	v_lshl_add_u64 v[220:221], v[216:217], 0, s[30:31]
	global_load_dwordx4 v[24:27], v[220:221], off
	global_load_dwordx4 v[28:31], v[220:221], off offset:64
	s_waitcnt vmcnt(12)
	v_fma_f32 v172, v124, v200, v172
	v_fma_f32 v173, v125, v201, v173
	v_fma_f32 v174, v126, v202, v174
	v_fma_f32 v175, v127, v203, v175
	v_fma_f32 v176, v120, v204, v176
	v_fma_f32 v177, v121, v205, v177
	v_fma_f32 v178, v122, v206, v178
	v_fma_f32 v179, v123, v207, v179
	v_cvt_pk_bf16_f32 v172, v172, v173
	v_cvt_pk_bf16_f32 v173, v174, v175
	v_cvt_pk_bf16_f32 v174, v176, v177
	v_cvt_pk_bf16_f32 v175, v178, v179
	s_mov_b32 s30, 0x40000
	s_mov_b32 s31, 0
	v_lshl_add_u64 v[222:223], v[218:219], 0, s[30:31]
	s_nop 1
	v_permlane32_swap_b32_e32 v172, v174
	v_permlane32_swap_b32_e32 v173, v175
	s_nop 1
	v_permlane16_swap_b32_e32 v172, v174
	v_permlane16_swap_b32_e32 v173, v175
	global_store_dwordx4 v[222:223], v[172:175], off
	s_mov_b32 s30, 0x200000
	s_mov_b32 s31, 0
	v_lshl_add_u64 v[220:221], v[216:217], 0, s[30:31]
	global_load_dwordx4 v[172:175], v[220:221], off offset:512
	global_load_dwordx4 v[176:179], v[220:221], off offset:576
	s_waitcnt vmcnt(12)
	v_fma_f32 v0, v108, v208, v0
	v_fma_f32 v1, v109, v209, v1
	v_fma_f32 v2, v110, v210, v2
	v_fma_f32 v3, v111, v211, v3
	v_fma_f32 v4, v104, v212, v4
	v_fma_f32 v5, v105, v213, v5
	v_fma_f32 v6, v106, v214, v6
	v_fma_f32 v7, v107, v215, v7
	v_cvt_pk_bf16_f32 v0, v0, v1
	v_cvt_pk_bf16_f32 v1, v2, v3
	v_cvt_pk_bf16_f32 v2, v4, v5
	v_cvt_pk_bf16_f32 v3, v6, v7
	s_mov_b32 s30, 0x40000
	s_mov_b32 s31, 0
	v_lshl_add_u64 v[222:223], v[218:219], 0, s[30:31]
	s_nop 1
	v_permlane32_swap_b32_e32 v0, v2
	v_permlane32_swap_b32_e32 v1, v3
	s_nop 1
	v_permlane16_swap_b32_e32 v0, v2
	v_permlane16_swap_b32_e32 v1, v3
	global_store_dwordx4 v[222:223], v[0:3], off offset:256
	s_mov_b32 s30, 0x240000
	s_mov_b32 s31, 0
	v_lshl_add_u64 v[220:221], v[216:217], 0, s[30:31]
	global_load_dwordx4 v[0:3], v[220:221], off
	global_load_dwordx4 v[4:7], v[220:221], off offset:64
	s_waitcnt vmcnt(12)
	v_fma_f32 v8, v116, v200, v8
	v_fma_f32 v9, v117, v201, v9
	v_fma_f32 v10, v118, v202, v10
	v_fma_f32 v11, v119, v203, v11
	v_fma_f32 v12, v112, v204, v12
	v_fma_f32 v13, v113, v205, v13
	v_fma_f32 v14, v114, v206, v14
	v_fma_f32 v15, v115, v207, v15
	v_cvt_pk_bf16_f32 v8, v8, v9
	v_cvt_pk_bf16_f32 v9, v10, v11
	v_cvt_pk_bf16_f32 v10, v12, v13
	v_cvt_pk_bf16_f32 v11, v14, v15
	s_mov_b32 s30, 0x60000
	s_mov_b32 s31, 0
	v_lshl_add_u64 v[222:223], v[218:219], 0, s[30:31]
	s_nop 1
	v_permlane32_swap_b32_e32 v8, v10
	v_permlane32_swap_b32_e32 v9, v11
	s_nop 1
	v_permlane16_swap_b32_e32 v8, v10
	v_permlane16_swap_b32_e32 v9, v11
	global_store_dwordx4 v[222:223], v[8:11], off
	s_mov_b32 s30, 0x240000
	s_mov_b32 s31, 0
	v_lshl_add_u64 v[220:221], v[216:217], 0, s[30:31]
	global_load_dwordx4 v[8:11], v[220:221], off offset:512
	global_load_dwordx4 v[12:15], v[220:221], off offset:576
	s_waitcnt vmcnt(12)
	v_fma_f32 v16, v100, v208, v16
	v_fma_f32 v17, v101, v209, v17
	v_fma_f32 v18, v102, v210, v18
	v_fma_f32 v19, v103, v211, v19
	v_fma_f32 v20, v96, v212, v20
	v_fma_f32 v21, v97, v213, v21
	v_fma_f32 v22, v98, v214, v22
	v_fma_f32 v23, v99, v215, v23
	v_cvt_pk_bf16_f32 v16, v16, v17
	v_cvt_pk_bf16_f32 v17, v18, v19
	v_cvt_pk_bf16_f32 v18, v20, v21
	v_cvt_pk_bf16_f32 v19, v22, v23
	s_mov_b32 s30, 0x60000
	s_mov_b32 s31, 0
	v_lshl_add_u64 v[222:223], v[218:219], 0, s[30:31]
	s_nop 1
	v_permlane32_swap_b32_e32 v16, v18
	v_permlane32_swap_b32_e32 v17, v19
	s_nop 1
	v_permlane16_swap_b32_e32 v16, v18
	v_permlane16_swap_b32_e32 v17, v19
	global_store_dwordx4 v[222:223], v[16:19], off offset:256
	s_mov_b32 s30, 0x280000
	s_mov_b32 s31, 0
	v_lshl_add_u64 v[220:221], v[216:217], 0, s[30:31]
	global_load_dwordx4 v[16:19], v[220:221], off
	global_load_dwordx4 v[20:23], v[220:221], off offset:64
	s_waitcnt vmcnt(12)
	v_fma_f32 v24, v92, v200, v24
	v_fma_f32 v25, v93, v201, v25
	v_fma_f32 v26, v94, v202, v26
	v_fma_f32 v27, v95, v203, v27
	v_fma_f32 v28, v88, v204, v28
	v_fma_f32 v29, v89, v205, v29
	v_fma_f32 v30, v90, v206, v30
	v_fma_f32 v31, v91, v207, v31
	v_cvt_pk_bf16_f32 v24, v24, v25
	v_cvt_pk_bf16_f32 v25, v26, v27
	v_cvt_pk_bf16_f32 v26, v28, v29
	v_cvt_pk_bf16_f32 v27, v30, v31
	s_mov_b32 s30, 0x100000
	s_mov_b32 s31, 0
	v_lshl_add_u64 v[222:223], v[218:219], 0, s[30:31]
	s_nop 1
	v_permlane32_swap_b32_e32 v24, v26
	v_permlane32_swap_b32_e32 v25, v27
	s_nop 1
	v_permlane16_swap_b32_e32 v24, v26
	v_permlane16_swap_b32_e32 v25, v27
	global_store_dwordx4 v[222:223], v[24:27], off
	s_mov_b32 s30, 0x280000
	s_mov_b32 s31, 0
	v_lshl_add_u64 v[220:221], v[216:217], 0, s[30:31]
	global_load_dwordx4 v[24:27], v[220:221], off offset:512
	global_load_dwordx4 v[28:31], v[220:221], off offset:576
	s_waitcnt vmcnt(12)
	v_fma_f32 v172, v76, v208, v172
	v_fma_f32 v173, v77, v209, v173
	v_fma_f32 v174, v78, v210, v174
	v_fma_f32 v175, v79, v211, v175
	v_fma_f32 v176, v72, v212, v176
	v_fma_f32 v177, v73, v213, v177
	v_fma_f32 v178, v74, v214, v178
	v_fma_f32 v179, v75, v215, v179
	v_cvt_pk_bf16_f32 v172, v172, v173
	v_cvt_pk_bf16_f32 v173, v174, v175
	v_cvt_pk_bf16_f32 v174, v176, v177
	v_cvt_pk_bf16_f32 v175, v178, v179
	s_mov_b32 s30, 0x100000
	s_mov_b32 s31, 0
	v_lshl_add_u64 v[222:223], v[218:219], 0, s[30:31]
	s_nop 1
	v_permlane32_swap_b32_e32 v172, v174
	v_permlane32_swap_b32_e32 v173, v175
	s_nop 1
	v_permlane16_swap_b32_e32 v172, v174
	v_permlane16_swap_b32_e32 v173, v175
	global_store_dwordx4 v[222:223], v[172:175], off offset:256
	s_mov_b32 s30, 0x2c0000
	s_mov_b32 s31, 0
	v_lshl_add_u64 v[220:221], v[216:217], 0, s[30:31]
	global_load_dwordx4 v[172:175], v[220:221], off
	global_load_dwordx4 v[176:179], v[220:221], off offset:64
	s_waitcnt vmcnt(12)
	v_fma_f32 v0, v84, v200, v0
	v_fma_f32 v1, v85, v201, v1
	v_fma_f32 v2, v86, v202, v2
	v_fma_f32 v3, v87, v203, v3
	v_fma_f32 v4, v80, v204, v4
	v_fma_f32 v5, v81, v205, v5
	v_fma_f32 v6, v82, v206, v6
	v_fma_f32 v7, v83, v207, v7
	v_cvt_pk_bf16_f32 v0, v0, v1
	v_cvt_pk_bf16_f32 v1, v2, v3
	v_cvt_pk_bf16_f32 v2, v4, v5
	v_cvt_pk_bf16_f32 v3, v6, v7
	s_mov_b32 s30, 0x120000
	s_mov_b32 s31, 0
	v_lshl_add_u64 v[222:223], v[218:219], 0, s[30:31]
	s_nop 1
	v_permlane32_swap_b32_e32 v0, v2
	v_permlane32_swap_b32_e32 v1, v3
	s_nop 1
	v_permlane16_swap_b32_e32 v0, v2
	v_permlane16_swap_b32_e32 v1, v3
	global_store_dwordx4 v[222:223], v[0:3], off
	s_mov_b32 s30, 0x2c0000
	s_mov_b32 s31, 0
	v_lshl_add_u64 v[220:221], v[216:217], 0, s[30:31]
	global_load_dwordx4 v[0:3], v[220:221], off offset:512
	global_load_dwordx4 v[4:7], v[220:221], off offset:576
	s_waitcnt vmcnt(12)
	v_fma_f32 v8, v68, v208, v8
	v_fma_f32 v9, v69, v209, v9
	v_fma_f32 v10, v70, v210, v10
	v_fma_f32 v11, v71, v211, v11
	v_fma_f32 v12, v64, v212, v12
	v_fma_f32 v13, v65, v213, v13
	v_fma_f32 v14, v66, v214, v14
	v_fma_f32 v15, v67, v215, v15
	v_cvt_pk_bf16_f32 v8, v8, v9
	v_cvt_pk_bf16_f32 v9, v10, v11
	v_cvt_pk_bf16_f32 v10, v12, v13
	v_cvt_pk_bf16_f32 v11, v14, v15
	s_mov_b32 s30, 0x120000
	s_mov_b32 s31, 0
	v_lshl_add_u64 v[222:223], v[218:219], 0, s[30:31]
	s_nop 1
	v_permlane32_swap_b32_e32 v8, v10
	v_permlane32_swap_b32_e32 v9, v11
	s_nop 1
	v_permlane16_swap_b32_e32 v8, v10
	v_permlane16_swap_b32_e32 v9, v11
	global_store_dwordx4 v[222:223], v[8:11], off offset:256
	s_waitcnt vmcnt(10)
	v_fma_f32 v16, v60, v200, v16
	v_fma_f32 v17, v61, v201, v17
	v_fma_f32 v18, v62, v202, v18
	v_fma_f32 v19, v63, v203, v19
	v_fma_f32 v20, v56, v204, v20
	v_fma_f32 v21, v57, v205, v21
	v_fma_f32 v22, v58, v206, v22
	v_fma_f32 v23, v59, v207, v23
	v_cvt_pk_bf16_f32 v16, v16, v17
	v_cvt_pk_bf16_f32 v17, v18, v19
	v_cvt_pk_bf16_f32 v18, v20, v21
	v_cvt_pk_bf16_f32 v19, v22, v23
	s_mov_b32 s30, 0x140000
	s_mov_b32 s31, 0
	v_lshl_add_u64 v[222:223], v[218:219], 0, s[30:31]
	s_nop 1
	v_permlane32_swap_b32_e32 v16, v18
	v_permlane32_swap_b32_e32 v17, v19
	s_nop 1
	v_permlane16_swap_b32_e32 v16, v18
	v_permlane16_swap_b32_e32 v17, v19
	global_store_dwordx4 v[222:223], v[16:19], off
	s_waitcnt vmcnt(8)
	v_fma_f32 v24, v44, v208, v24
	v_fma_f32 v25, v45, v209, v25
	v_fma_f32 v26, v46, v210, v26
	v_fma_f32 v27, v47, v211, v27
	v_fma_f32 v28, v40, v212, v28
	v_fma_f32 v29, v41, v213, v29
	v_fma_f32 v30, v42, v214, v30
	v_fma_f32 v31, v43, v215, v31
	v_cvt_pk_bf16_f32 v24, v24, v25
	v_cvt_pk_bf16_f32 v25, v26, v27
	v_cvt_pk_bf16_f32 v26, v28, v29
	v_cvt_pk_bf16_f32 v27, v30, v31
	s_mov_b32 s30, 0x140000
	s_mov_b32 s31, 0
	v_lshl_add_u64 v[222:223], v[218:219], 0, s[30:31]
	s_nop 1
	v_permlane32_swap_b32_e32 v24, v26
	v_permlane32_swap_b32_e32 v25, v27
	s_nop 1
	v_permlane16_swap_b32_e32 v24, v26
	v_permlane16_swap_b32_e32 v25, v27
	global_store_dwordx4 v[222:223], v[24:27], off offset:256
	s_waitcnt vmcnt(6)
	v_fma_f32 v172, v52, v200, v172
	v_fma_f32 v173, v53, v201, v173
	v_fma_f32 v174, v54, v202, v174
	v_fma_f32 v175, v55, v203, v175
	v_fma_f32 v176, v48, v204, v176
	v_fma_f32 v177, v49, v205, v177
	v_fma_f32 v178, v50, v206, v178
	v_fma_f32 v179, v51, v207, v179
	v_cvt_pk_bf16_f32 v172, v172, v173
	v_cvt_pk_bf16_f32 v173, v174, v175
	v_cvt_pk_bf16_f32 v174, v176, v177
	v_cvt_pk_bf16_f32 v175, v178, v179
	s_mov_b32 s30, 0x160000
	s_mov_b32 s31, 0
	v_lshl_add_u64 v[222:223], v[218:219], 0, s[30:31]
	s_nop 1
	v_permlane32_swap_b32_e32 v172, v174
	v_permlane32_swap_b32_e32 v173, v175
	s_nop 1
	v_permlane16_swap_b32_e32 v172, v174
	v_permlane16_swap_b32_e32 v173, v175
	global_store_dwordx4 v[222:223], v[172:175], off
	s_waitcnt vmcnt(4)
	v_fma_f32 v0, v36, v208, v0
	v_fma_f32 v1, v37, v209, v1
	v_fma_f32 v2, v38, v210, v2
	v_fma_f32 v3, v39, v211, v3
	v_fma_f32 v4, v32, v212, v4
	v_fma_f32 v5, v33, v213, v5
	v_fma_f32 v6, v34, v214, v6
	v_fma_f32 v7, v35, v215, v7
	v_cvt_pk_bf16_f32 v0, v0, v1
	v_cvt_pk_bf16_f32 v1, v2, v3
	v_cvt_pk_bf16_f32 v2, v4, v5
	v_cvt_pk_bf16_f32 v3, v6, v7
	s_mov_b32 s30, 0x160000
	s_mov_b32 s31, 0
	v_lshl_add_u64 v[222:223], v[218:219], 0, s[30:31]
	s_nop 1
	v_permlane32_swap_b32_e32 v0, v2
	v_permlane32_swap_b32_e32 v1, v3
	s_nop 1
	v_permlane16_swap_b32_e32 v0, v2
	v_permlane16_swap_b32_e32 v1, v3
	global_store_dwordx4 v[222:223], v[0:3], off offset:256
	s_cbranch_vccnz .LBB0_554
	s_andn2_b64 vcc, exec, s[10:11]
	s_cbranch_vccnz .LBB0_553
	s_barrier
	s_branch .LBB0_553
